# scores phase: XCD-aware unit order (the 4 head units of a row panel on one XCD) on top of v24
# baseline (speedup 1.0000x reference)
; template <class Epi, class Sched, bool GATHER, bool LIGHTSKIP = false>
; __device__ __forceinline__ void gemm_phase(LAS unsigned char* lds, LAS unsigned char* xl, const int lda, const int ldb, const int K, const Sched& S, const Epi& E) {
;     ...
;     GUnit cur, nxt; int ui = 0;
;     if (!S.next(0, cur)) return;
;     Acc acc;
;     __device__ __forceinline__ bool next(int i, GUnit& u) const {
;         const int L = i * G + c; if (L >= 512) return false;
;         const int pm = L >> 2, h = L & 3, b = pm >> 6;
;         u.pm = pm; u.pn = h; u.A = S1 + (size_t)pm * 256 * 2048 * 2; u.B = MT + ((size_t)(b * 1024 + h * 256) * 2048) * 2; u.x0 = pm * 256; u.x1 = h * 256; return true;
.LBB0_927:
	s_or_b64 exec, exec, s[10:11]
	s_waitcnt lgkmcnt(0)
	s_barrier
	s_load_dwordx2 s[10:11], s[70:71], 0xd8
	v_mov_b32_e32 v10, v0
	s_waitcnt lgkmcnt(0)
	s_and_b32 s101, s92, 7
	s_lshl_b32 s101, s101, 5
	s_lshr_b32 s100, s92, 3
	s_or_b32 s101, s101, s100
	s_cmp_eq_u32 s94, 0x100
	s_cselect_b32 s101, s101, s92
	s_add_u32 s0, s10, 0x24010000
	s_addc_u32 s1, s11, 0
	s_add_u32 s2, s10, 0x2c010000
	s_addc_u32 s3, s11, 0
	s_cmpk_lt_i32 s101, 0x200
	s_cselect_b64 s[12:13], -1, 0
	s_cmpk_gt_i32 s101, 0x1ff
	v_readfirstlane_b32 s36, v10
	s_cbranch_scc1 .LBB0_929
	s_ashr_i32 s60, s101, 2
	s_ashr_i32 s61, s60, 31
	s_and_b32 s83, s101, 3
	s_lshl_b64 s[4:5], s[60:61], 20
	s_add_u32 s62, s0, s4
	s_addc_u32 s63, s1, s5
	s_lshl_b32 s4, s101, 2
	s_and_b32 s4, s4, 0xfffffc00
	s_lshl_b32 s61, s83, 8
	s_or_b32 s4, s4, s61
	s_ashr_i32 s5, s4, 31
	s_lshl_b64 s[4:5], s[4:5], 12
	s_add_u32 s64, s2, s4
	s_addc_u32 s65, s3, s5
	s_lshl_b32 s82, s60, 8
	s_andn2_b64 vcc, exec, s[12:13]
	s_cbranch_vccz .LBB0_930
	s_branch .LBB0_964

; template <class Epi, class Sched, bool GATHER, bool LIGHTSKIP = false>
; __device__ __forceinline__ void gemm_phase(LAS unsigned char* lds, LAS unsigned char* xl, const int lda, const int ldb, const int K, const Sched& S, const Epi& E) {
;     ...
;         const bool has_next = S.next(ui + 1, nxt);
;         const char* nA = has_next ? nxt.A : cA; const char* nB = has_next ? nxt.B : cB;
;     __device__ __forceinline__ bool next(int i, GUnit& u) const {
;         const int L = i * G + c; if (L >= 512) return false;
;         const int pm = L >> 2, h = L & 3, b = pm >> 6;
;         u.pm = pm; u.pn = h; u.A = S1 + (size_t)pm * 256 * 2048 * 2; u.B = MT + ((size_t)(b * 1024 + h * 256) * 2048) * 2; u.x0 = pm * 256; u.x1 = h * 256; return true;
.LBB0_935:
	s_add_i32 s27, s27, 1
	s_mul_i32 s66, s27, s94
	s_add_i32 s66, s66, s101
	s_cmpk_lt_i32 s66, 0x200
	s_cselect_b64 s[58:59], -1, 0
	s_cmpk_gt_i32 s66, 0x1ff
	s_cbranch_scc1 .LBB0_937
	s_ashr_i32 s52, s66, 2
	s_ashr_i32 s53, s52, 31
	s_and_b32 s80, s66, 3
	s_lshl_b64 s[54:55], s[52:53], 20
	s_add_u32 s54, s0, s54
	s_addc_u32 s55, s1, s55
	s_lshl_b32 s53, s66, 2
	s_and_b32 s56, s53, 0xfffffc00
	s_lshl_b32 s53, s80, 8
	s_or_b32 s56, s56, s53
	s_ashr_i32 s57, s56, 31
	s_lshl_b64 s[56:57], s[56:57], 12
	s_add_u32 s56, s2, s56
	s_addc_u32 s57, s3, s57
	s_lshl_b32 s81, s52, 8
